# norm+dt row loops: loop-top vmcnt(0) moved to preheader, exact rotation waits (no per-row store drain)
# speedup vs baseline: 1.0074x; 1.0074x over previous
.LBB0_227:
	s_load_dwordx2 s[0:1], s[16:17], 0xa0
	s_load_dwordx2 s[4:5], s[16:17], 0x10
	s_waitcnt vmcnt(15)
	v_or_b32_e32 v2, 1, v129
	s_movk_i32 s3, 0x6420
	v_lshlrev_b32_e32 v208, 4, v200
	s_waitcnt lgkmcnt(0)
	s_add_u32 s0, s0, s18
	s_addc_u32 s1, s1, s19
	s_add_u32 s4, s4, s81
	s_addc_u32 s5, s5, s80
	v_mov_b64_e32 v[0:1], s[4:5]
	s_waitcnt vmcnt(11)
	v_mad_u64_u32 v[18:19], s[4:5], v2, s3, v[0:1]
	v_or_b32_e32 v2, 2, v129
	s_waitcnt vmcnt(7)
	v_mad_u64_u32 v[32:33], s[4:5], v2, s3, v[0:1]
	v_or_b32_e32 v2, 3, v129
	v_mad_u64_u32 v[34:35], s[4:5], v2, s3, v[0:1]
	v_add_u32_e32 v2, 0x100, v129
	v_mad_u64_u32 v[48:49], s[4:5], v2, s3, v[0:1]
	v_add_u32_e32 v2, 0x101, v129
	v_mad_u64_u32 v[50:51], s[4:5], v2, s3, v[0:1]
	v_add_u32_e32 v2, 0x102, v129
	v_mad_u64_u32 v[64:65], s[4:5], v2, s3, v[0:1]
	v_add_u32_e32 v2, 0x103, v129
	v_mad_u64_u32 v[66:67], s[4:5], v2, s3, v[0:1]
	v_or_b32_e32 v2, 0x200, v129
	s_waitcnt vmcnt(1)
	v_mad_u64_u32 v[80:81], s[4:5], v2, s3, v[0:1]
	v_add_u32_e32 v2, 0x201, v129
	v_mad_u64_u32 v[82:83], s[4:5], v2, s3, v[0:1]
	v_add_u32_e32 v2, 0x202, v129
	v_mad_u64_u32 v[96:97], s[4:5], v2, s3, v[0:1]
	v_add_u32_e32 v2, 0x203, v129
	v_mad_u64_u32 v[98:99], s[4:5], v2, s3, v[0:1]
	v_add_u32_e32 v2, 0x300, v129
	v_mad_u64_u32 v[112:113], s[4:5], v2, s3, v[0:1]
	v_add_u32_e32 v2, 0x301, v129
	v_mad_u64_u32 v[114:115], s[4:5], v2, s3, v[0:1]
	v_add_u32_e32 v2, 0x302, v129
	v_mad_u64_u32 v[130:131], s[4:5], v2, s3, v[0:1]
	v_add_u32_e32 v2, 0x303, v129
	v_mad_u64_u32 v[16:17], s[4:5], v129, s3, v[0:1]
	s_mov_b64 s[6:7], 0x3400
	v_mad_u64_u32 v[128:129], s[4:5], v2, s3, v[0:1]
	global_load_dwordx4 v[0:3], v208, s[0:1]
	global_load_dwordx4 v[4:7], v208, s[0:1] offset:1024
	global_load_dwordx4 v[8:11], v208, s[0:1] offset:2048
	global_load_dwordx4 v[12:15], v208, s[0:1] offset:3072
	s_movk_i32 s0, 0x3000
	v_lshl_add_u64 v[24:25], v[16:17], 0, s[6:7]
	v_add_co_u32_e32 v16, vcc, s0, v16
	v_lshl_add_u64 v[40:41], v[32:33], 0, s[6:7]
	s_nop 0
	v_addc_co_u32_e32 v17, vcc, 0, v17, vcc
	v_add_co_u32_e32 v20, vcc, s0, v18
	v_lshl_add_u64 v[56:57], v[48:49], 0, s[6:7]
	s_nop 0
	v_addc_co_u32_e32 v21, vcc, 0, v19, vcc
	v_add_co_u32_e32 v32, vcc, s0, v32
	v_lshl_add_u64 v[72:73], v[64:65], 0, s[6:7]
	s_nop 0
	v_addc_co_u32_e32 v33, vcc, 0, v33, vcc
	v_add_co_u32_e32 v36, vcc, s0, v34
	v_lshl_add_u64 v[88:89], v[80:81], 0, s[6:7]
	s_nop 0
	v_addc_co_u32_e32 v37, vcc, 0, v35, vcc
	v_add_co_u32_e32 v48, vcc, s0, v48
	v_lshl_add_u64 v[104:105], v[96:97], 0, s[6:7]
	s_nop 0
	v_addc_co_u32_e32 v49, vcc, 0, v49, vcc
	v_add_co_u32_e32 v52, vcc, s0, v50
	v_lshl_add_u64 v[120:121], v[112:113], 0, s[6:7]
	s_nop 0
	v_addc_co_u32_e32 v53, vcc, 0, v51, vcc
	v_add_co_u32_e32 v64, vcc, s0, v64
	v_lshl_add_u64 v[136:137], v[130:131], 0, s[6:7]
	s_nop 0
	v_addc_co_u32_e32 v65, vcc, 0, v65, vcc
	v_add_co_u32_e32 v68, vcc, s0, v66
	v_lshl_add_u64 v[28:29], v[18:19], 0, s[6:7]
	s_nop 0
	v_addc_co_u32_e32 v69, vcc, 0, v67, vcc
	v_add_co_u32_e32 v80, vcc, s0, v80
	v_lshl_add_u64 v[44:45], v[34:35], 0, s[6:7]
	s_nop 0
	v_addc_co_u32_e32 v81, vcc, 0, v81, vcc
	s_waitcnt vmcnt(4)
	v_add_co_u32_e32 v84, vcc, s0, v82
	v_lshl_add_u64 v[60:61], v[50:51], 0, s[6:7]
	s_nop 0
	v_addc_co_u32_e32 v85, vcc, 0, v83, vcc
	v_add_co_u32_e32 v96, vcc, s0, v96
	v_lshl_add_u64 v[76:77], v[66:67], 0, s[6:7]
	s_nop 0
	v_addc_co_u32_e32 v97, vcc, 0, v97, vcc
	v_add_co_u32_e32 v100, vcc, s0, v98
	v_lshl_add_u64 v[92:93], v[82:83], 0, s[6:7]
	s_nop 0
	v_addc_co_u32_e32 v101, vcc, 0, v99, vcc
	v_add_co_u32_e32 v112, vcc, s0, v112
	v_lshl_add_u64 v[108:109], v[98:99], 0, s[6:7]
	s_nop 0
	v_addc_co_u32_e32 v113, vcc, 0, v113, vcc
	v_add_co_u32_e32 v116, vcc, s0, v114
	v_lshl_add_u64 v[124:125], v[114:115], 0, s[6:7]
	s_nop 0
	v_addc_co_u32_e32 v117, vcc, 0, v115, vcc
	v_add_co_u32_e32 v130, vcc, s0, v130
	v_lshl_add_u64 v[140:141], v[128:129], 0, s[6:7]
	s_nop 0
	v_addc_co_u32_e32 v131, vcc, 0, v131, vcc
	v_add_co_u32_e32 v132, vcc, 0x3000, v128
	global_load_dwordx4 v[16:19], v[16:17], off offset:1024
	s_nop 0
	global_load_dwordx4 v[20:23], v[20:21], off offset:1024
	s_nop 0
	global_load_dwordx4 v[24:27], v[24:25], off offset:16
	s_nop 0
	global_load_dwordx4 v[28:31], v[28:29], off offset:16
	v_addc_co_u32_e32 v133, vcc, 0, v129, vcc
	global_load_dwordx4 v[32:35], v[32:33], off offset:1024
	s_nop 0
	global_load_dwordx4 v[36:39], v[36:37], off offset:1024
	s_nop 0
	global_load_dwordx4 v[40:43], v[40:41], off offset:16
	s_nop 0
	global_load_dwordx4 v[44:47], v[44:45], off offset:16
	s_nop 0
	global_load_dwordx4 v[48:51], v[48:49], off offset:1024
	s_nop 0
	global_load_dwordx4 v[52:55], v[52:53], off offset:1024
	s_nop 0
	global_load_dwordx4 v[56:59], v[56:57], off offset:16
	s_nop 0
	global_load_dwordx4 v[60:63], v[60:61], off offset:16
	s_nop 0
	global_load_dwordx4 v[64:67], v[64:65], off offset:1024
	s_nop 0
	global_load_dwordx4 v[68:71], v[68:69], off offset:1024
	s_nop 0
	global_load_dwordx4 v[72:75], v[72:73], off offset:16
	s_nop 0
	global_load_dwordx4 v[76:79], v[76:77], off offset:16
	s_nop 0
	global_load_dwordx4 v[80:83], v[80:81], off offset:1024
	s_nop 0
	global_load_dwordx4 v[84:87], v[84:85], off offset:1024
	s_nop 0
	global_load_dwordx4 v[88:91], v[88:89], off offset:16
	s_nop 0
	global_load_dwordx4 v[92:95], v[92:93], off offset:16
	s_nop 0
	global_load_dwordx4 v[96:99], v[96:97], off offset:1024
	s_nop 0
	global_load_dwordx4 v[100:103], v[100:101], off offset:1024
	s_nop 0
	global_load_dwordx4 v[104:107], v[104:105], off offset:16
	s_nop 0
	global_load_dwordx4 v[108:111], v[108:109], off offset:16
	s_nop 0
	global_load_dwordx4 v[112:115], v[112:113], off offset:1024
	s_nop 0
	global_load_dwordx4 v[116:119], v[116:117], off offset:1024
	s_nop 0
	global_load_dwordx4 v[120:123], v[120:121], off offset:16
	s_nop 0
	global_load_dwordx4 v[124:127], v[124:125], off offset:16
	s_nop 0
	global_load_dwordx4 v[128:131], v[130:131], off offset:1024
	s_nop 0
	global_load_dwordx4 v[132:135], v[132:133], off offset:1024
	s_nop 0
	global_load_dwordx4 v[136:139], v[136:137], off offset:16
	s_nop 0
	global_load_dwordx4 v[140:143], v[140:141], off offset:16
	s_add_i32 s0, s14, 0xb40
	s_add_i32 s1, s20, 0xfffffec0
	s_cmpk_lt_i32 s14, 0x140
	s_cselect_b32 s22, s14, s0
	s_cselect_b32 s24, 0x140, s1
	s_movk_i32 s0, 0xc80
	s_cselect_b32 s15, s0, 0x8000
	s_add_i32 s0, s24, s22
	s_cmp_lt_i32 s0, s15
	s_cselect_b32 s28, s0, s22
	s_ashr_i32 s23, s22, 31
	s_ashr_i32 s29, s28, 31
	s_lshl_b64 s[26:27], s[22:23], 11
	s_lshl_b32 s21, s24, 1
	s_cmp_lt_i32 s22, s15
	v_lshrrev_b16_e32 v144, 4, v200
	s_cselect_b64 s[8:9], -1, 0
	v_lshrrev_b16_e32 v145, 3, v200
	v_and_b32_e32 v144, 1, v144
	v_and_b32_e32 v174, 1, v145
	v_cmp_eq_u32_e64 s[0:1], 1, v144
	v_cmp_lt_i32_e64 s[6:7], 31, v200
	v_cndmask_b32_e64 v144, 0, 1, s[8:9]
	s_cmp_lg_u32 s2, 0
	v_cmp_eq_u32_e64 s[2:3], 1, v174
	v_cmp_eq_u32_e64 s[4:5], 0, v152
	v_cndmask_b32_e64 v175, 0, 4, s[6:7]
	v_cmp_ne_u32_e64 s[8:9], 1, v144
	s_cbranch_scc0 .LBB0_234
	s_and_b64 vcc, exec, s[8:9]
	s_mov_b32 s38, 0x4500000
	s_cbranch_vccnz .LBB0_233
	s_add_u32 s10, s12, 0x26d00000
	s_addc_u32 s11, s13, 0
	s_lshl_b64 s[30:31], s[28:29], 11
	s_add_u32 s30, s10, s30
	v_lshlrev_b32_e32 v156, 3, v200
	v_mov_b32_e32 v157, v209
	s_addc_u32 s31, s11, s31
	v_lshl_add_u64 v[144:145], s[10:11], 0, v[156:157]
	s_add_u32 s10, s10, s26
	s_addc_u32 s11, s11, s27
	global_load_dwordx2 v[146:147], v156, s[30:31] offset:1536
	global_load_dwordx2 v[148:149], v156, s[30:31] offset:1024
	global_load_dwordx2 v[150:151], v156, s[30:31] offset:512
	global_load_dwordx2 v[152:153], v156, s[30:31]
	global_load_dwordx2 v[170:171], v156, s[10:11] offset:1536
	global_load_dwordx2 v[166:167], v156, s[10:11] offset:1024
	global_load_dwordx2 v[168:169], v156, s[10:11] offset:512
	global_load_dwordx2 v[172:173], v156, s[10:11]
	v_and_b32_e32 v154, 64, v225
	v_add_u32_e32 v154, 64, v154
	v_xor_b32_e32 v155, 1, v225
	v_cmp_lt_i32_e32 vcc, v155, v154
	s_lshl_b64 s[10:11], s[22:23], 5
	s_add_u32 s10, s10, 0x25d00000
	v_cndmask_b32_e32 v155, v225, v155, vcc
	v_lshlrev_b32_e32 v176, 2, v155
	v_xor_b32_e32 v155, 2, v225
	v_cmp_lt_i32_e32 vcc, v155, v154
	s_addc_u32 s11, s11, 0
	v_lshlrev_b32_e32 v158, 2, v175
	v_cndmask_b32_e32 v155, v225, v155, vcc
	v_lshlrev_b32_e32 v177, 2, v155
	v_xor_b32_e32 v155, 4, v225
	v_cmp_lt_i32_e32 vcc, v155, v154
	v_mov_b32_e32 v159, v209
	s_ashr_i32 s25, s24, 31
	v_cndmask_b32_e32 v155, v225, v155, vcc
	v_lshlrev_b32_e32 v178, 2, v155
	v_xor_b32_e32 v155, 8, v225
	v_cmp_lt_i32_e32 vcc, v155, v154
	s_lshl_b64 s[30:31], s[24:25], 5
	v_lshl_add_u64 v[156:157], s[26:27], 0, v[156:157]
	v_cndmask_b32_e32 v155, v225, v155, vcc
	v_lshlrev_b32_e32 v179, 2, v155
	v_xor_b32_e32 v155, 16, v225
	v_cmp_lt_i32_e32 vcc, v155, v154
	s_lshl_b64 s[34:35], s[24:25], 11
	s_mov_b32 s25, s22
	v_cndmask_b32_e32 v155, v225, v155, vcc
	v_lshlrev_b32_e32 v180, 2, v155
	v_xor_b32_e32 v155, 32, v225
	v_cmp_lt_i32_e32 vcc, v155, v154
	s_nop 1
	v_cndmask_b32_e32 v154, v225, v155, vcc
	v_lshlrev_b32_e32 v181, 2, v154
	v_cndmask_b32_e64 v154, 0, 1, s[0:1]
	v_lshl_or_b32 v154, v154, 3, s10
	v_mov_b32_e32 v155, s11
	v_lshl_add_u64 v[154:155], v[154:155], 0, v[158:159]
	v_mov_b32_e32 v158, 2
	v_lshlrev_b32_sdwa v158, v158, v174 dst_sel:DWORD dst_unused:UNUSED_PAD src0_sel:DWORD src1_sel:WORD_0
	v_lshl_add_u64 v[154:155], v[154:155], 0, v[158:159]
	s_waitcnt vmcnt(0)
	s_branch .LBB0_231
.LBB0_230:
	s_or_b64 exec, exec, s[10:11]
	s_add_i32 s25, s25, s24
	v_lshl_add_u64 v[154:155], v[154:155], 0, s[30:31]
	v_lshl_add_u64 v[156:157], v[156:157], 0, s[34:35]
	s_cmp_lt_i32 s25, s15
	v_mov_b64_e32 v[170:171], v[146:147]
	s_waitcnt lgkmcnt(0)
	v_mov_b64_e32 v[166:167], v[148:149]
	v_mov_b64_e32 v[168:169], v[150:151]
	v_mov_b64_e32 v[172:173], v[152:153]
	s_waitcnt vmcnt(5)
	v_mov_b64_e32 v[146:147], v[164:165]
	v_mov_b64_e32 v[148:149], v[162:163]
	v_mov_b64_e32 v[150:151], v[160:161]
	v_mov_b64_e32 v[152:153], v[158:159]
	s_cbranch_scc0 .LBB0_233
.LBB0_231:
	v_lshlrev_b32_e32 v187, 16, v173
	v_lshlrev_b32_e32 v186, 16, v172
	v_and_b32_e32 v173, 0xffff0000, v173
	v_and_b32_e32 v172, 0xffff0000, v172
	v_pk_mul_f32 v[188:189], v[172:173], v[172:173]
	v_lshlrev_b32_e32 v191, 16, v169
	v_pk_fma_f32 v[188:189], v[186:187], v[186:187], v[188:189]
	v_lshlrev_b32_e32 v190, 16, v168
	v_and_b32_e32 v169, 0xffff0000, v169
	v_and_b32_e32 v168, 0xffff0000, v168
	v_lshlrev_b32_e32 v182, 16, v166
	v_and_b32_e32 v183, 0xffff0000, v166
	v_lshlrev_b32_e32 v184, 16, v170
	v_pk_add_f32 v[188:189], v[188:189], v[188:189] op_sel_hi:[0,1]
	v_pk_mul_f32 v[192:193], v[168:169], v[168:169]
	v_lshlrev_b32_e32 v166, 16, v167
	v_pk_fma_f32 v[192:193], v[190:191], v[190:191], v[192:193]
	v_mul_f32_e32 v185, v182, v182
	v_mul_f32_e32 v195, v183, v183
	v_and_b32_e32 v167, 0xffff0000, v167
	v_mul_f32_e32 v188, v166, v166
	v_mov_b32_e32 v194, v184
	v_and_b32_e32 v201, 0xffff0000, v170
	v_lshlrev_b32_e32 v170, 16, v171
	v_and_b32_e32 v171, 0xffff0000, v171
	v_pk_add_f32 v[192:193], v[192:193], v[192:193] op_sel_hi:[0,1]
	v_pk_fma_f32 v[196:197], v[166:167], v[166:167], v[188:189] op_sel_hi:[1,1,0]
	v_pk_add_f32 v[194:195], v[184:185], v[194:195]
	v_mul_f32_e32 v196, v201, v201
	v_mul_f32_e32 v192, v170, v170
	v_mul_f32_e32 v188, v171, v171
	v_mul_f32_e32 v198, v184, v184
	v_mov_b32_e32 v199, v195
	v_pk_add_f32 v[194:195], v[198:199], v[196:197]
	v_pk_add_f32 v[188:189], v[192:193], v[188:189]
	s_add_i32 s10, s21, s25
	v_pk_add_f32 v[188:189], v[194:195], v[188:189]
	s_cmp_lt_i32 s10, s15
	v_add_f32_e32 v185, v188, v189
	ds_bpermute_b32 v188, v176, v185
	s_cselect_b32 s10, s10, s25
	s_ashr_i32 s11, s10, 31
	s_lshl_b64 s[10:11], s[10:11], 11
	v_lshl_add_u64 v[164:165], v[144:145], 0, s[10:11]
	s_waitcnt lgkmcnt(0)
	v_add_f32_e32 v185, v185, v188
	ds_bpermute_b32 v188, v177, v185
	global_load_dwordx2 v[158:159], v[164:165], off
	global_load_dwordx2 v[160:161], v[164:165], off offset:512
	global_load_dwordx2 v[162:163], v[164:165], off offset:1024
	s_nop 0
	global_load_dwordx2 v[164:165], v[164:165], off offset:1536
	v_mov_b32_e32 v195, v172
	v_mov_b32_e32 v172, v187
	s_waitcnt lgkmcnt(0)
	v_add_f32_e32 v185, v185, v188
	ds_bpermute_b32 v188, v178, v185
	s_waitcnt lgkmcnt(0)
	v_add_f32_e32 v185, v185, v188
	ds_bpermute_b32 v188, v179, v185
	s_waitcnt lgkmcnt(0)
	v_add_f32_e32 v185, v185, v188
	ds_bpermute_b32 v188, v180, v185
	s_waitcnt lgkmcnt(0)
	v_add_f32_e32 v185, v185, v188
	ds_bpermute_b32 v188, v181, v185
	s_waitcnt lgkmcnt(0)
	v_add_f32_e32 v185, v185, v188
	v_fmamk_f32 v185, v185, 0x3a800000, v222
	v_cmp_gt_f32_e32 vcc, s78, v185
	v_mul_f32_e32 v188, 0x4f800000, v185
	s_nop 0
	v_cndmask_b32_e32 v185, v185, v188, vcc
	v_sqrt_f32_e32 v188, v185
	s_nop 0
	v_add_u32_e32 v189, -1, v188
	v_fma_f32 v192, -v189, v188, v185
	v_cmp_ge_f32_e64 s[10:11], 0, v192
	v_add_u32_e32 v192, 1, v188
	s_nop 0
	v_cndmask_b32_e64 v189, v188, v189, s[10:11]
	v_fma_f32 v188, -v192, v188, v185
	v_cmp_lt_f32_e64 s[10:11], 0, v188
	s_nop 1
	v_cndmask_b32_e64 v188, v189, v192, s[10:11]
	v_mul_f32_e32 v189, 0x37800000, v188
	v_cndmask_b32_e32 v188, v188, v189, vcc
	v_cmp_class_f32_e32 vcc, v185, v223
	s_nop 1
	v_cndmask_b32_e32 v185, v188, v185, vcc
	v_div_scale_f32 v188, s[10:11], v185, v185, 1.0
	v_rcp_f32_e32 v189, v188
	s_nop 0
	v_fma_f32 v192, -v188, v189, 1.0
	v_fmac_f32_e32 v189, v192, v189
	v_div_scale_f32 v192, vcc, 1.0, v185, 1.0
	v_mul_f32_e32 v193, v192, v189
	v_fma_f32 v194, -v188, v193, v192
	v_fmac_f32_e32 v193, v194, v189
	v_fma_f32 v188, -v188, v193, v192
	v_div_fmas_f32 v188, v188, v189, v193
	v_div_fixup_f32 v188, v188, v185, 1.0
	v_mov_b32_e32 v194, v186
	v_lshl_add_u64 v[192:193], s[12:13], 0, v[156:157]
	v_pk_mul_f32 v[194:195], v[188:189], v[194:195] op_sel_hi:[0,1]
	v_pk_mul_f32 v[172:173], v[188:189], v[172:173] op_sel_hi:[0,1]
	v_pk_mul_f32 v[172:173], v[2:3], v[172:173]
	v_pk_mul_f32 v[186:187], v[0:1], v[194:195]
	v_add_co_u32_e32 v192, vcc, s38, v192
	v_cvt_pk_bf16_f32 v194, v186, v187
	v_cvt_pk_bf16_f32 v195, v172, v173
	v_addc_co_u32_e32 v193, vcc, 0, v193, vcc
	global_store_dwordx2 v[192:193], v[194:195], off
	v_mov_b32_e32 v194, v190
	v_mov_b32_e32 v195, v168
	v_mov_b32_e32 v168, v191
	v_pk_mul_f32 v[194:195], v[188:189], v[194:195] op_sel_hi:[0,1]
	v_pk_mul_f32 v[168:169], v[188:189], v[168:169] op_sel_hi:[0,1]
	v_mov_b32_e32 v185, v201
	v_pk_mul_f32 v[168:169], v[6:7], v[168:169]
	v_pk_mul_f32 v[190:191], v[4:5], v[194:195]
	v_pk_mul_f32 v[182:183], v[182:183], v[188:189] op_sel_hi:[1,0]
	v_pk_mul_f32 v[166:167], v[166:167], v[188:189] op_sel_hi:[1,0]
	v_pk_mul_f32 v[184:185], v[184:185], v[188:189] op_sel_hi:[1,0]
	v_pk_mul_f32 v[170:171], v[170:171], v[188:189] op_sel_hi:[1,0]
	v_cvt_pk_bf16_f32 v194, v190, v191
	v_cvt_pk_bf16_f32 v195, v168, v169
	v_pk_mul_f32 v[166:167], v[10:11], v[166:167]
	v_pk_mul_f32 v[182:183], v[8:9], v[182:183]
	v_pk_mul_f32 v[170:171], v[14:15], v[170:171]
	v_pk_mul_f32 v[184:185], v[12:13], v[184:185]
	global_store_dwordx2 v[192:193], v[194:195], off offset:512
	v_cvt_pk_bf16_f32 v194, v182, v183
	v_cvt_pk_bf16_f32 v195, v166, v167
	v_cvt_pk_bf16_f32 v188, v184, v185
	v_cvt_pk_bf16_f32 v189, v170, v171
	global_store_dwordx2 v[192:193], v[194:195], off offset:1024
	global_store_dwordx2 v[192:193], v[188:189], off offset:1536
	v_pk_fma_f32 v[188:189], v[16:17], v[186:187], 0 op_sel_hi:[1,0,0]
	v_pk_fma_f32 v[192:193], v[18:19], v[186:187], 0 op_sel_hi:[1,0,0]
	v_pk_fma_f32 v[194:195], v[24:25], v[186:187], 0 op_sel_hi:[1,0,0]
	v_pk_fma_f32 v[196:197], v[26:27], v[186:187], 0 op_sel_hi:[1,0,0]
	v_pk_fma_f32 v[192:193], v[22:23], v[186:187], v[192:193] op_sel:[0,1,0]
	v_pk_fma_f32 v[188:189], v[20:21], v[186:187], v[188:189] op_sel:[0,1,0]
	v_pk_fma_f32 v[196:197], v[30:31], v[186:187], v[196:197] op_sel:[0,1,0]
	v_pk_fma_f32 v[186:187], v[28:29], v[186:187], v[194:195] op_sel:[0,1,0]
	v_pk_fma_f32 v[188:189], v[32:33], v[172:173], v[188:189] op_sel_hi:[1,0,1]
	v_pk_fma_f32 v[192:193], v[34:35], v[172:173], v[192:193] op_sel_hi:[1,0,1]
	v_pk_fma_f32 v[186:187], v[40:41], v[172:173], v[186:187] op_sel_hi:[1,0,1]
	v_pk_fma_f32 v[194:195], v[42:43], v[172:173], v[196:197] op_sel_hi:[1,0,1]
	v_pk_fma_f32 v[192:193], v[38:39], v[172:173], v[192:193] op_sel:[0,1,0]
	v_pk_fma_f32 v[188:189], v[36:37], v[172:173], v[188:189] op_sel:[0,1,0]
	v_pk_fma_f32 v[194:195], v[46:47], v[172:173], v[194:195] op_sel:[0,1,0]
	v_pk_fma_f32 v[172:173], v[44:45], v[172:173], v[186:187] op_sel:[0,1,0]
	v_pk_fma_f32 v[186:187], v[48:49], v[190:191], v[188:189] op_sel_hi:[1,0,1]
	v_pk_fma_f32 v[188:189], v[50:51], v[190:191], v[192:193] op_sel_hi:[1,0,1]
	v_pk_fma_f32 v[172:173], v[56:57], v[190:191], v[172:173] op_sel_hi:[1,0,1]
	v_pk_fma_f32 v[192:193], v[58:59], v[190:191], v[194:195] op_sel_hi:[1,0,1]
	v_pk_fma_f32 v[188:189], v[54:55], v[190:191], v[188:189] op_sel:[0,1,0]
	v_pk_fma_f32 v[186:187], v[52:53], v[190:191], v[186:187] op_sel:[0,1,0]
	v_pk_fma_f32 v[192:193], v[62:63], v[190:191], v[192:193] op_sel:[0,1,0]
	v_pk_fma_f32 v[172:173], v[60:61], v[190:191], v[172:173] op_sel:[0,1,0]
	v_pk_fma_f32 v[186:187], v[64:65], v[168:169], v[186:187] op_sel_hi:[1,0,1]
	v_pk_fma_f32 v[188:189], v[66:67], v[168:169], v[188:189] op_sel_hi:[1,0,1]
	v_pk_fma_f32 v[172:173], v[72:73], v[168:169], v[172:173] op_sel_hi:[1,0,1]
	v_pk_fma_f32 v[190:191], v[74:75], v[168:169], v[192:193] op_sel_hi:[1,0,1]
	v_pk_fma_f32 v[188:189], v[70:71], v[168:169], v[188:189] op_sel:[0,1,0]
	v_pk_fma_f32 v[186:187], v[68:69], v[168:169], v[186:187] op_sel:[0,1,0]
	v_pk_fma_f32 v[190:191], v[78:79], v[168:169], v[190:191] op_sel:[0,1,0]
	v_pk_fma_f32 v[168:169], v[76:77], v[168:169], v[172:173] op_sel:[0,1,0]
	v_pk_fma_f32 v[172:173], v[80:81], v[182:183], v[186:187] op_sel_hi:[1,0,1]
	v_pk_fma_f32 v[186:187], v[82:83], v[182:183], v[188:189] op_sel_hi:[1,0,1]
	v_pk_fma_f32 v[168:169], v[88:89], v[182:183], v[168:169] op_sel_hi:[1,0,1]
	v_pk_fma_f32 v[188:189], v[90:91], v[182:183], v[190:191] op_sel_hi:[1,0,1]
	v_pk_fma_f32 v[186:187], v[86:87], v[182:183], v[186:187] op_sel:[0,1,0]
	v_pk_fma_f32 v[172:173], v[84:85], v[182:183], v[172:173] op_sel:[0,1,0]
	v_pk_fma_f32 v[188:189], v[94:95], v[182:183], v[188:189] op_sel:[0,1,0]
	v_pk_fma_f32 v[168:169], v[92:93], v[182:183], v[168:169] op_sel:[0,1,0]
	v_pk_fma_f32 v[172:173], v[96:97], v[166:167], v[172:173] op_sel_hi:[1,0,1]
	v_pk_fma_f32 v[182:183], v[98:99], v[166:167], v[186:187] op_sel_hi:[1,0,1]
	v_pk_fma_f32 v[168:169], v[104:105], v[166:167], v[168:169] op_sel_hi:[1,0,1]
	v_pk_fma_f32 v[186:187], v[106:107], v[166:167], v[188:189] op_sel_hi:[1,0,1]
	v_pk_fma_f32 v[182:183], v[102:103], v[166:167], v[182:183] op_sel:[0,1,0]
	v_pk_fma_f32 v[172:173], v[100:101], v[166:167], v[172:173] op_sel:[0,1,0]
	v_pk_fma_f32 v[186:187], v[110:111], v[166:167], v[186:187] op_sel:[0,1,0]
	v_pk_fma_f32 v[166:167], v[108:109], v[166:167], v[168:169] op_sel:[0,1,0]
	v_pk_fma_f32 v[168:169], v[112:113], v[184:185], v[172:173] op_sel_hi:[1,0,1]
	v_pk_fma_f32 v[166:167], v[120:121], v[184:185], v[166:167] op_sel_hi:[1,0,1]
	v_pk_fma_f32 v[172:173], v[114:115], v[184:185], v[182:183] op_sel_hi:[1,0,1]
	v_pk_fma_f32 v[182:183], v[122:123], v[184:185], v[186:187] op_sel_hi:[1,0,1]
	v_pk_fma_f32 v[168:169], v[116:117], v[184:185], v[168:169] op_sel:[0,1,0]
	v_pk_fma_f32 v[166:167], v[124:125], v[184:185], v[166:167] op_sel:[0,1,0]
	v_pk_fma_f32 v[172:173], v[118:119], v[184:185], v[172:173] op_sel:[0,1,0]
	v_pk_fma_f32 v[182:183], v[126:127], v[184:185], v[182:183] op_sel:[0,1,0]
	v_pk_fma_f32 v[168:169], v[128:129], v[170:171], v[168:169] op_sel_hi:[1,0,1]
	v_pk_fma_f32 v[166:167], v[136:137], v[170:171], v[166:167] op_sel_hi:[1,0,1]
	v_pk_fma_f32 v[172:173], v[130:131], v[170:171], v[172:173] op_sel_hi:[1,0,1]
	v_pk_fma_f32 v[182:183], v[138:139], v[170:171], v[182:183] op_sel_hi:[1,0,1]
	v_pk_fma_f32 v[168:169], v[132:133], v[170:171], v[168:169] op_sel:[0,1,0]
	v_pk_fma_f32 v[166:167], v[140:141], v[170:171], v[166:167] op_sel:[0,1,0]
	v_pk_fma_f32 v[172:173], v[134:135], v[170:171], v[172:173] op_sel:[0,1,0]
	v_pk_fma_f32 v[182:183], v[142:143], v[170:171], v[182:183] op_sel:[0,1,0]
	v_cndmask_b32_e64 v170, v168, v166, s[6:7]
	v_cndmask_b32_e64 v166, v166, v168, s[6:7]
	ds_bpermute_b32 v166, v181, v166
	v_cndmask_b32_e64 v168, v169, v167, s[6:7]
	v_cndmask_b32_e64 v167, v167, v169, s[6:7]
	ds_bpermute_b32 v167, v181, v167
	v_cndmask_b32_e64 v169, v182, v172, s[6:7]
	s_waitcnt lgkmcnt(1)
	v_add_f32_e32 v166, v170, v166
	ds_bpermute_b32 v169, v181, v169
	v_cndmask_b32_e64 v170, v183, v173, s[6:7]
	ds_bpermute_b32 v170, v181, v170
	s_waitcnt lgkmcnt(2)
	v_add_f32_e32 v167, v168, v167
	v_cndmask_b32_e64 v168, v172, v182, s[6:7]
	s_waitcnt lgkmcnt(1)
	v_add_f32_e32 v168, v168, v169
	v_cndmask_b32_e64 v169, v173, v183, s[6:7]
	s_waitcnt lgkmcnt(0)
	v_add_f32_e32 v169, v169, v170
	v_cndmask_b32_e64 v170, v166, v168, s[0:1]
	v_cndmask_b32_e64 v166, v168, v166, s[0:1]
	v_cndmask_b32_e64 v168, v167, v169, s[0:1]
	v_cndmask_b32_e64 v167, v169, v167, s[0:1]
	ds_bpermute_b32 v166, v180, v166
	ds_bpermute_b32 v167, v180, v167
	s_waitcnt lgkmcnt(1)
	v_add_f32_e32 v166, v170, v166
	s_waitcnt lgkmcnt(0)
	v_add_f32_e32 v167, v168, v167
	v_cndmask_b32_e64 v168, v166, v167, s[2:3]
	v_cndmask_b32_e64 v166, v167, v166, s[2:3]
	ds_bpermute_b32 v166, v179, v166
	s_waitcnt lgkmcnt(0)
	v_add_f32_e32 v166, v168, v166
	ds_bpermute_b32 v167, v178, v166
	s_waitcnt lgkmcnt(0)
	v_add_f32_e32 v166, v166, v167
	ds_bpermute_b32 v167, v177, v166
	s_waitcnt lgkmcnt(0)
	v_add_f32_e32 v166, v166, v167
	ds_bpermute_b32 v167, v176, v166
	s_and_saveexec_b64 s[10:11], s[4:5]
	s_cbranch_execz .LBB0_230
	v_lshl_add_u64 v[168:169], s[12:13], 0, v[154:155]
	s_waitcnt lgkmcnt(0)
	v_add_f32_e32 v166, v166, v167
	global_store_dword v[168:169], v166, off
	s_branch .LBB0_230

.LBB0_235:
	s_and_b64 vcc, exec, s[8:9]
	s_cbranch_vccnz .LBB0_240
	s_load_dwordx2 s[8:9], s[16:17], 0x0
	s_lshl_b64 s[10:11], s[28:29], 12
	v_and_b32_e32 v160, 64, v225
	v_add_u32_e32 v160, 64, v160
	v_xor_b32_e32 v161, 1, v225
	s_waitcnt lgkmcnt(0)
	s_add_u32 s10, s8, s10
	s_addc_u32 s11, s9, s11
	s_lshl_b64 s[28:29], s[22:23], 12
	s_add_u32 s28, s8, s28
	global_load_dwordx4 v[156:159], v208, s[10:11] offset:3072
	global_load_dwordx4 v[152:155], v208, s[10:11] offset:2048
	s_addc_u32 s29, s9, s29
	global_load_dwordx4 v[148:151], v208, s[10:11] offset:1024
	global_load_dwordx4 v[144:147], v208, s[10:11]
	global_load_dwordx4 v[176:179], v208, s[28:29] offset:3072
	global_load_dwordx4 v[180:183], v208, s[28:29] offset:2048
	global_load_dwordx4 v[184:187], v208, s[28:29] offset:1024
	global_load_dwordx4 v[188:191], v208, s[28:29]
	v_cmp_lt_i32_e32 vcc, v161, v160
	v_lshl_add_u64 v[192:193], s[8:9], 0, v[208:209]
	s_lshl_b64 s[8:9], s[22:23], 5
	v_cndmask_b32_e32 v161, v225, v161, vcc
	v_lshlrev_b32_e32 v201, 2, v161
	v_xor_b32_e32 v161, 2, v225
	v_cmp_lt_i32_e32 vcc, v161, v160
	s_add_u32 s8, s8, 0x25d00000
	s_addc_u32 s9, s9, 0
	v_cndmask_b32_e32 v161, v225, v161, vcc
	v_lshlrev_b32_e32 v202, 2, v161
	v_xor_b32_e32 v161, 4, v225
	v_cmp_lt_i32_e32 vcc, v161, v160
	v_lshlrev_b32_e32 v162, 2, v175
	v_mov_b32_e32 v163, v209
	v_cndmask_b32_e32 v161, v225, v161, vcc
	v_lshlrev_b32_e32 v203, 2, v161
	v_xor_b32_e32 v161, 8, v225
	v_cmp_lt_i32_e32 vcc, v161, v160
	s_ashr_i32 s25, s24, 31
	s_lshl_b64 s[10:11], s[24:25], 5
	v_cndmask_b32_e32 v161, v225, v161, vcc
	v_lshlrev_b32_e32 v204, 2, v161
	v_xor_b32_e32 v161, 16, v225
	v_cmp_lt_i32_e32 vcc, v161, v160
	s_nop 1
	v_cndmask_b32_e32 v161, v225, v161, vcc
	v_lshlrev_b32_e32 v205, 2, v161
	v_xor_b32_e32 v161, 32, v225
	v_cmp_lt_i32_e32 vcc, v161, v160
	s_nop 1
	v_cndmask_b32_e32 v160, v225, v161, vcc
	v_lshlrev_b32_e32 v206, 2, v160
	v_cndmask_b32_e64 v160, 0, 1, s[0:1]
	v_lshl_or_b32 v160, v160, 3, s8
	v_mov_b32_e32 v161, s9
	v_lshl_add_u64 v[160:161], v[160:161], 0, v[162:163]
	v_mov_b32_e32 v162, 2
	v_lshlrev_b32_sdwa v162, v162, v174 dst_sel:DWORD dst_unused:UNUSED_PAD src0_sel:DWORD src1_sel:WORD_0
	v_lshl_add_u64 v[194:195], v[160:161], 0, v[162:163]
	v_lshlrev_b32_e32 v160, 3, v200
	v_mov_b32_e32 v161, v209
	v_lshl_add_u64 v[196:197], s[26:27], 0, v[160:161]
	s_lshl_b64 s[26:27], s[24:25], 11
	s_waitcnt vmcnt(0)
	s_branch .LBB0_238
.LBB0_237:
	s_or_b64 exec, exec, s[8:9]
	v_mov_b32_e32 v176, v156
	s_waitcnt lgkmcnt(0)
	v_mov_b32_e32 v177, v157
	v_mov_b32_e32 v178, v158
	v_mov_b32_e32 v179, v159
	v_mov_b32_e32 v180, v152
	v_mov_b32_e32 v181, v153
	v_mov_b32_e32 v182, v154
	v_mov_b32_e32 v183, v155
	v_mov_b32_e32 v184, v148
	v_mov_b32_e32 v185, v149
	v_mov_b32_e32 v186, v150
	v_mov_b32_e32 v187, v151
	v_mov_b32_e32 v188, v144
	v_mov_b32_e32 v189, v145
	v_mov_b32_e32 v190, v146
	v_mov_b32_e32 v191, v147
	s_add_i32 s22, s22, s24
	s_waitcnt vmcnt(12)
	v_mov_b64_e32 v[144:145], v[160:161]
	s_waitcnt vmcnt(11)
	v_mov_b64_e32 v[148:149], v[164:165]
	s_waitcnt vmcnt(10)
	v_mov_b64_e32 v[152:153], v[168:169]
	s_waitcnt vmcnt(9)
	v_mov_b64_e32 v[156:157], v[172:173]
	v_lshl_add_u64 v[194:195], v[194:195], 0, s[10:11]
	v_lshl_add_u64 v[196:197], v[196:197], 0, s[26:27]
	s_cmp_ge_i32 s22, s15
	v_mov_b64_e32 v[146:147], v[162:163]
	v_mov_b64_e32 v[150:151], v[166:167]
	v_mov_b64_e32 v[154:155], v[170:171]
	v_mov_b64_e32 v[158:159], v[174:175]
	s_cbranch_scc1 .LBB0_240
.LBB0_238:
	s_add_i32 s8, s21, s22
	s_cmp_lt_i32 s8, s15
	s_cselect_b32 s8, s8, s22
	s_ashr_i32 s9, s8, 31
	s_lshl_b64 s[8:9], s[8:9], 12
	v_lshl_add_u64 v[172:173], v[192:193], 0, s[8:9]
	v_lshl_add_u64 v[198:199], s[12:13], 0, v[196:197]
	s_mov_b32 s8, 0x26d00000
	v_add_co_u32_e32 v212, vcc, s8, v198
	v_cvt_pk_bf16_f32 v210, v188, v189
	v_cvt_pk_bf16_f32 v211, v190, v191
	v_addc_co_u32_e32 v213, vcc, 0, v199, vcc
	global_load_dwordx4 v[160:163], v[172:173], off
	global_load_dwordx4 v[164:167], v[172:173], off offset:1024
	global_load_dwordx4 v[168:171], v[172:173], off offset:2048
	s_nop 0
	global_load_dwordx4 v[172:175], v[172:173], off offset:3072
	v_pk_mul_f32 v[214:215], v[190:191], v[190:191]
	global_store_dwordx2 v[212:213], v[210:211], off
	v_cvt_pk_bf16_f32 v210, v184, v185
	v_cvt_pk_bf16_f32 v211, v186, v187
	global_store_dwordx2 v[212:213], v[210:211], off offset:512
	v_cvt_pk_bf16_f32 v210, v180, v181
	v_cvt_pk_bf16_f32 v211, v182, v183
	global_store_dwordx2 v[212:213], v[210:211], off offset:1024
	v_cvt_pk_bf16_f32 v210, v176, v177
	v_cvt_pk_bf16_f32 v211, v178, v179
	v_pk_mul_f32 v[216:217], v[188:189], v[188:189]
	global_store_dwordx2 v[212:213], v[210:211], off offset:1536
	v_pk_mul_f32 v[210:211], v[186:187], v[186:187]
	v_pk_mul_f32 v[212:213], v[184:185], v[184:185]
	v_pk_mov_b32 v[218:219], v[216:217], v[214:215] op_sel:[1,0]
	v_mov_b32_e32 v217, v215
	v_pk_add_f32 v[214:215], v[218:219], v[216:217]
	v_pk_mov_b32 v[216:217], v[212:213], v[210:211] op_sel:[1,0]
	v_mov_b32_e32 v213, v211
	v_pk_add_f32 v[210:211], v[216:217], v[212:213]
	v_pk_add_f32 v[214:215], v[214:215], v[214:215] op_sel_hi:[0,1]
	v_pk_add_f32 v[210:211], v[210:211], v[210:211] op_sel_hi:[0,1]
	v_mul_f32_e32 v210, v180, v180
	v_pk_fma_f32 v[212:213], v[180:181], v[180:181], v[210:211] op_sel_hi:[1,1,0]
	v_mul_f32_e32 v210, v182, v182
	v_pk_fma_f32 v[216:217], v[182:183], v[182:183], v[210:211] op_sel_hi:[1,1,0]
	v_mul_f32_e32 v212, v176, v176
	v_mul_f32_e32 v216, v177, v177
	v_mul_f32_e32 v214, v178, v178
	v_mul_f32_e32 v210, v179, v179
	v_pk_add_f32 v[212:213], v[212:213], v[216:217]
	v_pk_add_f32 v[210:211], v[214:215], v[210:211]
	s_nop 0
	v_pk_add_f32 v[210:211], v[212:213], v[210:211]
	s_nop 0
	v_add_f32_e32 v207, v210, v211
	ds_bpermute_b32 v210, v201, v207
	s_waitcnt lgkmcnt(0)
	v_add_f32_e32 v207, v207, v210
	ds_bpermute_b32 v210, v202, v207
	s_waitcnt lgkmcnt(0)
	v_add_f32_e32 v207, v207, v210
	ds_bpermute_b32 v210, v203, v207
	s_waitcnt lgkmcnt(0)
	v_add_f32_e32 v207, v207, v210
	ds_bpermute_b32 v210, v204, v207
	s_waitcnt lgkmcnt(0)
	v_add_f32_e32 v207, v207, v210
	ds_bpermute_b32 v210, v205, v207
	s_waitcnt lgkmcnt(0)
	v_add_f32_e32 v207, v207, v210
	ds_bpermute_b32 v210, v206, v207
	s_waitcnt lgkmcnt(0)
	v_add_f32_e32 v207, v207, v210
	v_fmamk_f32 v207, v207, 0x3a800000, v222
	v_cmp_gt_f32_e32 vcc, s78, v207
	v_mul_f32_e32 v210, 0x4f800000, v207
	s_nop 0
	v_cndmask_b32_e32 v207, v207, v210, vcc
	v_sqrt_f32_e32 v210, v207
	s_nop 0
	v_add_u32_e32 v211, -1, v210
	v_fma_f32 v212, -v211, v210, v207
	v_cmp_ge_f32_e64 s[8:9], 0, v212
	v_add_u32_e32 v212, 1, v210
	s_nop 0
	v_cndmask_b32_e64 v211, v210, v211, s[8:9]
	v_fma_f32 v210, -v212, v210, v207
	v_cmp_lt_f32_e64 s[8:9], 0, v210
	s_nop 1
	v_cndmask_b32_e64 v210, v211, v212, s[8:9]
	v_mul_f32_e32 v211, 0x37800000, v210
	v_cndmask_b32_e32 v210, v210, v211, vcc
	v_cmp_class_f32_e32 vcc, v207, v223
	s_nop 1
	v_cndmask_b32_e32 v207, v210, v207, vcc
	v_div_scale_f32 v210, s[8:9], v207, v207, 1.0
	v_rcp_f32_e32 v211, v210
	s_nop 0
	v_fma_f32 v212, -v210, v211, 1.0
	v_fmac_f32_e32 v211, v212, v211
	v_div_scale_f32 v212, vcc, 1.0, v207, 1.0
	v_mul_f32_e32 v213, v212, v211
	v_fma_f32 v214, -v210, v213, v212
	v_fmac_f32_e32 v213, v214, v211
	v_fma_f32 v210, -v210, v213, v212
	v_div_fmas_f32 v210, v210, v211, v213
	v_div_fixup_f32 v210, v210, v207, 1.0
	v_pk_mul_f32 v[188:189], v[188:189], v[210:211] op_sel_hi:[1,0]
	v_pk_mul_f32 v[190:191], v[190:191], v[210:211] op_sel_hi:[1,0]
	v_pk_mul_f32 v[188:189], v[0:1], v[188:189]
	v_pk_mul_f32 v[190:191], v[2:3], v[190:191]
	v_add_co_u32_e32 v198, vcc, s38, v198
	v_pk_mul_f32 v[184:185], v[184:185], v[210:211] op_sel_hi:[1,0]
	v_pk_mul_f32 v[186:187], v[186:187], v[210:211] op_sel_hi:[1,0]
	v_cvt_pk_bf16_f32 v212, v188, v189
	v_cvt_pk_bf16_f32 v213, v190, v191
	v_addc_co_u32_e32 v199, vcc, 0, v199, vcc
	v_pk_mul_f32 v[186:187], v[6:7], v[186:187]
	v_pk_mul_f32 v[184:185], v[4:5], v[184:185]
	v_pk_mul_f32 v[180:181], v[180:181], v[210:211] op_sel_hi:[1,0]
	v_pk_mul_f32 v[182:183], v[182:183], v[210:211] op_sel_hi:[1,0]
	v_pk_mul_f32 v[176:177], v[176:177], v[210:211] op_sel_hi:[1,0]
	v_pk_mul_f32 v[178:179], v[178:179], v[210:211] op_sel_hi:[1,0]
	global_store_dwordx2 v[198:199], v[212:213], off
	v_cvt_pk_bf16_f32 v212, v184, v185
	v_cvt_pk_bf16_f32 v213, v186, v187
	v_pk_mul_f32 v[182:183], v[10:11], v[182:183]
	v_pk_mul_f32 v[180:181], v[8:9], v[180:181]
	v_pk_mul_f32 v[178:179], v[14:15], v[178:179]
	v_pk_mul_f32 v[176:177], v[12:13], v[176:177]
	global_store_dwordx2 v[198:199], v[212:213], off offset:512
	v_cvt_pk_bf16_f32 v212, v180, v181
	v_cvt_pk_bf16_f32 v213, v182, v183
	v_cvt_pk_bf16_f32 v210, v176, v177
	v_cvt_pk_bf16_f32 v211, v178, v179
	global_store_dwordx2 v[198:199], v[212:213], off offset:1024
	global_store_dwordx2 v[198:199], v[210:211], off offset:1536
	v_pk_fma_f32 v[198:199], v[16:17], v[188:189], 0 op_sel_hi:[1,0,0]
	v_pk_fma_f32 v[210:211], v[18:19], v[188:189], 0 op_sel_hi:[1,0,0]
	v_pk_fma_f32 v[212:213], v[24:25], v[188:189], 0 op_sel_hi:[1,0,0]
	v_pk_fma_f32 v[214:215], v[26:27], v[188:189], 0 op_sel_hi:[1,0,0]
	v_pk_fma_f32 v[210:211], v[22:23], v[188:189], v[210:211] op_sel:[0,1,0]
	v_pk_fma_f32 v[198:199], v[20:21], v[188:189], v[198:199] op_sel:[0,1,0]
	v_pk_fma_f32 v[214:215], v[30:31], v[188:189], v[214:215] op_sel:[0,1,0]
	v_pk_fma_f32 v[188:189], v[28:29], v[188:189], v[212:213] op_sel:[0,1,0]
	v_pk_fma_f32 v[198:199], v[32:33], v[190:191], v[198:199] op_sel_hi:[1,0,1]
	v_pk_fma_f32 v[210:211], v[34:35], v[190:191], v[210:211] op_sel_hi:[1,0,1]
	v_pk_fma_f32 v[188:189], v[40:41], v[190:191], v[188:189] op_sel_hi:[1,0,1]
	v_pk_fma_f32 v[212:213], v[42:43], v[190:191], v[214:215] op_sel_hi:[1,0,1]
	v_pk_fma_f32 v[210:211], v[38:39], v[190:191], v[210:211] op_sel:[0,1,0]
	v_pk_fma_f32 v[198:199], v[36:37], v[190:191], v[198:199] op_sel:[0,1,0]
	v_pk_fma_f32 v[212:213], v[46:47], v[190:191], v[212:213] op_sel:[0,1,0]
	v_pk_fma_f32 v[188:189], v[44:45], v[190:191], v[188:189] op_sel:[0,1,0]
	v_pk_fma_f32 v[190:191], v[48:49], v[184:185], v[198:199] op_sel_hi:[1,0,1]
	v_pk_fma_f32 v[198:199], v[50:51], v[184:185], v[210:211] op_sel_hi:[1,0,1]
	v_pk_fma_f32 v[188:189], v[56:57], v[184:185], v[188:189] op_sel_hi:[1,0,1]
	v_pk_fma_f32 v[210:211], v[58:59], v[184:185], v[212:213] op_sel_hi:[1,0,1]
	v_pk_fma_f32 v[198:199], v[54:55], v[184:185], v[198:199] op_sel:[0,1,0]
	v_pk_fma_f32 v[190:191], v[52:53], v[184:185], v[190:191] op_sel:[0,1,0]
	v_pk_fma_f32 v[210:211], v[62:63], v[184:185], v[210:211] op_sel:[0,1,0]
	v_pk_fma_f32 v[184:185], v[60:61], v[184:185], v[188:189] op_sel:[0,1,0]
	v_pk_fma_f32 v[188:189], v[64:65], v[186:187], v[190:191] op_sel_hi:[1,0,1]
	v_pk_fma_f32 v[190:191], v[66:67], v[186:187], v[198:199] op_sel_hi:[1,0,1]
	v_pk_fma_f32 v[184:185], v[72:73], v[186:187], v[184:185] op_sel_hi:[1,0,1]
	v_pk_fma_f32 v[198:199], v[74:75], v[186:187], v[210:211] op_sel_hi:[1,0,1]
	v_pk_fma_f32 v[190:191], v[70:71], v[186:187], v[190:191] op_sel:[0,1,0]
	v_pk_fma_f32 v[188:189], v[68:69], v[186:187], v[188:189] op_sel:[0,1,0]
	v_pk_fma_f32 v[198:199], v[78:79], v[186:187], v[198:199] op_sel:[0,1,0]
	v_pk_fma_f32 v[184:185], v[76:77], v[186:187], v[184:185] op_sel:[0,1,0]
	v_pk_fma_f32 v[186:187], v[80:81], v[180:181], v[188:189] op_sel_hi:[1,0,1]
	v_pk_fma_f32 v[188:189], v[82:83], v[180:181], v[190:191] op_sel_hi:[1,0,1]
	v_pk_fma_f32 v[184:185], v[88:89], v[180:181], v[184:185] op_sel_hi:[1,0,1]
	v_pk_fma_f32 v[190:191], v[90:91], v[180:181], v[198:199] op_sel_hi:[1,0,1]
	v_pk_fma_f32 v[188:189], v[86:87], v[180:181], v[188:189] op_sel:[0,1,0]
	v_pk_fma_f32 v[186:187], v[84:85], v[180:181], v[186:187] op_sel:[0,1,0]
	v_pk_fma_f32 v[190:191], v[94:95], v[180:181], v[190:191] op_sel:[0,1,0]
	v_pk_fma_f32 v[180:181], v[92:93], v[180:181], v[184:185] op_sel:[0,1,0]
	v_pk_fma_f32 v[184:185], v[96:97], v[182:183], v[186:187] op_sel_hi:[1,0,1]
	v_pk_fma_f32 v[186:187], v[98:99], v[182:183], v[188:189] op_sel_hi:[1,0,1]
	v_pk_fma_f32 v[180:181], v[104:105], v[182:183], v[180:181] op_sel_hi:[1,0,1]
	v_pk_fma_f32 v[188:189], v[106:107], v[182:183], v[190:191] op_sel_hi:[1,0,1]
	v_pk_fma_f32 v[186:187], v[102:103], v[182:183], v[186:187] op_sel:[0,1,0]
	v_pk_fma_f32 v[184:185], v[100:101], v[182:183], v[184:185] op_sel:[0,1,0]
	v_pk_fma_f32 v[188:189], v[110:111], v[182:183], v[188:189] op_sel:[0,1,0]
	v_pk_fma_f32 v[180:181], v[108:109], v[182:183], v[180:181] op_sel:[0,1,0]
	v_pk_fma_f32 v[182:183], v[112:113], v[176:177], v[184:185] op_sel_hi:[1,0,1]
	v_pk_fma_f32 v[184:185], v[114:115], v[176:177], v[186:187] op_sel_hi:[1,0,1]
	v_pk_fma_f32 v[180:181], v[120:121], v[176:177], v[180:181] op_sel_hi:[1,0,1]
	v_pk_fma_f32 v[186:187], v[122:123], v[176:177], v[188:189] op_sel_hi:[1,0,1]
	v_pk_fma_f32 v[184:185], v[118:119], v[176:177], v[184:185] op_sel:[0,1,0]
	v_pk_fma_f32 v[182:183], v[116:117], v[176:177], v[182:183] op_sel:[0,1,0]
	v_pk_fma_f32 v[186:187], v[126:127], v[176:177], v[186:187] op_sel:[0,1,0]
	v_pk_fma_f32 v[176:177], v[124:125], v[176:177], v[180:181] op_sel:[0,1,0]
	v_pk_fma_f32 v[180:181], v[128:129], v[178:179], v[182:183] op_sel_hi:[1,0,1]
	v_pk_fma_f32 v[176:177], v[136:137], v[178:179], v[176:177] op_sel_hi:[1,0,1]
	v_pk_fma_f32 v[182:183], v[130:131], v[178:179], v[184:185] op_sel_hi:[1,0,1]
	v_pk_fma_f32 v[184:185], v[138:139], v[178:179], v[186:187] op_sel_hi:[1,0,1]
	v_pk_fma_f32 v[180:181], v[132:133], v[178:179], v[180:181] op_sel:[0,1,0]
	v_pk_fma_f32 v[176:177], v[140:141], v[178:179], v[176:177] op_sel:[0,1,0]
	v_pk_fma_f32 v[182:183], v[134:135], v[178:179], v[182:183] op_sel:[0,1,0]
	v_pk_fma_f32 v[184:185], v[142:143], v[178:179], v[184:185] op_sel:[0,1,0]
	v_cndmask_b32_e64 v178, v180, v176, s[6:7]
	v_cndmask_b32_e64 v176, v176, v180, s[6:7]
	ds_bpermute_b32 v176, v206, v176
	v_cndmask_b32_e64 v179, v184, v182, s[6:7]
	ds_bpermute_b32 v179, v206, v179
	v_cndmask_b32_e64 v180, v185, v183, s[6:7]
	ds_bpermute_b32 v180, v206, v180
	s_waitcnt lgkmcnt(2)
	v_add_f32_e32 v176, v178, v176
	v_cndmask_b32_e64 v178, v181, v177, s[6:7]
	v_cndmask_b32_e64 v177, v177, v181, s[6:7]
	ds_bpermute_b32 v177, v206, v177
	s_waitcnt lgkmcnt(0)
	v_add_f32_e32 v177, v178, v177
	v_cndmask_b32_e64 v178, v182, v184, s[6:7]
	v_add_f32_e32 v178, v178, v179
	v_cndmask_b32_e64 v179, v183, v185, s[6:7]
	v_add_f32_e32 v179, v179, v180
	v_cndmask_b32_e64 v180, v176, v178, s[0:1]
	v_cndmask_b32_e64 v176, v178, v176, s[0:1]
	v_cndmask_b32_e64 v178, v177, v179, s[0:1]
	v_cndmask_b32_e64 v177, v179, v177, s[0:1]
	ds_bpermute_b32 v176, v205, v176
	ds_bpermute_b32 v177, v205, v177
	s_waitcnt lgkmcnt(1)
	v_add_f32_e32 v176, v180, v176
	s_waitcnt lgkmcnt(0)
	v_add_f32_e32 v177, v178, v177
	v_cndmask_b32_e64 v178, v176, v177, s[2:3]
	v_cndmask_b32_e64 v176, v177, v176, s[2:3]
	ds_bpermute_b32 v176, v204, v176
	s_waitcnt lgkmcnt(0)
	v_add_f32_e32 v176, v178, v176
	ds_bpermute_b32 v177, v203, v176
	s_waitcnt lgkmcnt(0)
	v_add_f32_e32 v176, v176, v177
	ds_bpermute_b32 v177, v202, v176
	s_waitcnt lgkmcnt(0)
	v_add_f32_e32 v176, v176, v177
	ds_bpermute_b32 v177, v201, v176
	s_and_saveexec_b64 s[8:9], s[4:5]
	s_cbranch_execz .LBB0_237
	v_lshl_add_u64 v[178:179], s[12:13], 0, v[194:195]
	s_waitcnt lgkmcnt(0)
	v_add_f32_e32 v176, v176, v177
	global_store_dword v[178:179], v176, off
	s_branch .LBB0_237
